# cache-policy: post / Hyena / branch-norm single-use row loads non-temporal
# baseline (speedup 1.0000x reference)
.LBB0_774:
	v_add_co_u32_e32 v18, vcc, 0xfffff000, v28
	s_nop 1
	v_addc_co_u32_e32 v19, vcc, -1, v29, vcc
	global_load_dwordx4 v[36:39], v[18:19], off offset:-16 nt
	global_load_dwordx4 v[44:47], v[28:29], off offset:-4096 nt
	s_nop 0
	global_load_dwordx4 v[18:21], v[28:29], off nt
	global_load_dwordx4 v[22:25], v[28:29], off offset:-16 nt
	s_waitcnt vmcnt(3)
	v_lshlrev_b32_e32 v32, 16, v36
	v_and_b32_e32 v33, 0xffff0000, v36
	v_lshlrev_b32_e32 v34, 16, v37
	v_and_b32_e32 v35, 0xffff0000, v37
	v_lshlrev_b32_e32 v36, 16, v38
	v_and_b32_e32 v37, 0xffff0000, v38
	v_lshlrev_b32_e32 v38, 16, v39
	v_and_b32_e32 v39, 0xffff0000, v39
	s_waitcnt vmcnt(2)
	v_lshlrev_b32_e32 v40, 16, v44
	v_and_b32_e32 v41, 0xffff0000, v44
	v_lshlrev_b32_e32 v42, 16, v45
	v_and_b32_e32 v43, 0xffff0000, v45
	v_lshlrev_b32_e32 v44, 16, v46
	v_and_b32_e32 v45, 0xffff0000, v46
	v_and_b32_e32 v30, 0xffff0000, v47
	v_lshlrev_b32_e32 v31, 16, v47
	s_and_saveexec_b64 s[12:13], s[6:7]
	s_cbranch_execz .LBB0_776
	v_pk_mul_f32 v[46:47], v[32:33], v[32:33]
	v_pk_mul_f32 v[48:49], v[34:35], v[34:35]
	v_add_f32_e32 v0, v46, v47
	v_add_f32_e32 v0, v48, v0
	v_pk_mul_f32 v[50:51], v[36:37], v[36:37]
	v_add_f32_e32 v0, v49, v0
	v_add_f32_e32 v0, v50, v0
	v_pk_mul_f32 v[58:59], v[38:39], v[38:39]
	v_add_f32_e32 v0, v51, v0
	v_add_f32_e32 v0, v58, v0
	v_pk_mul_f32 v[60:61], v[40:41], v[40:41]
	v_add_f32_e32 v0, v59, v0
	v_add_f32_e32 v0, v60, v0
	v_pk_mul_f32 v[62:63], v[42:43], v[42:43]
	v_add_f32_e32 v0, v61, v0
	v_add_f32_e32 v0, v62, v0
	v_pk_mul_f32 v[64:65], v[44:45], v[44:45]
	v_add_f32_e32 v0, v63, v0
	v_add_f32_e32 v0, v64, v0
	v_pk_mul_f32 v[66:67], v[30:31], v[30:31]
	v_add_f32_e32 v0, v65, v0
	v_add_f32_e32 v0, v67, v0
	v_add_f32_e32 v0, v66, v0
	v_mov_b32_e32 v46, 0x358637bd
	s_nop 0
	v_add_f32_dpp v0, v0, v0 quad_perm:[1,0,3,2] row_mask:0xf bank_mask:0xf bound_ctrl:1
	s_nop 1
	v_add_f32_dpp v0, v0, v0 quad_perm:[2,3,0,1] row_mask:0xf bank_mask:0xf bound_ctrl:1
	v_fmamk_f32 v0, v0, 0x3c800000, v46
	v_mul_f32_e32 v27, 0x4b800000, v0
	v_cmp_gt_f32_e32 vcc, s59, v0
	s_nop 1
	v_cndmask_b32_e32 v0, v0, v27, vcc
	v_rsq_f32_e32 v0, v0
	s_nop 0
	v_mul_f32_e32 v27, 0x45800000, v0
	v_cndmask_b32_e32 v0, v0, v27, vcc
	v_pk_mul_f32 v[30:31], v[0:1], v[30:31] op_sel_hi:[0,1]
	v_pk_mul_f32 v[32:33], v[0:1], v[32:33] op_sel_hi:[0,1]
	v_pk_mul_f32 v[34:35], v[0:1], v[34:35] op_sel_hi:[0,1]
	v_pk_mul_f32 v[36:37], v[0:1], v[36:37] op_sel_hi:[0,1]
	v_pk_mul_f32 v[38:39], v[0:1], v[38:39] op_sel_hi:[0,1]
	v_pk_mul_f32 v[40:41], v[0:1], v[40:41] op_sel_hi:[0,1]
	v_pk_mul_f32 v[42:43], v[0:1], v[42:43] op_sel_hi:[0,1]
	v_pk_mul_f32 v[44:45], v[0:1], v[44:45] op_sel_hi:[0,1]
	v_pk_mul_f32 v[46:47], v[4:5], v[30:31] op_sel:[0,1] op_sel_hi:[1,0]
	v_pk_mul_f32 v[32:33], v[14:15], v[32:33]
	v_pk_mul_f32 v[34:35], v[16:17], v[34:35]
	v_pk_mul_f32 v[36:37], v[10:11], v[36:37]
	v_pk_mul_f32 v[38:39], v[12:13], v[38:39]
	v_pk_mul_f32 v[40:41], v[6:7], v[40:41]
	v_pk_mul_f32 v[42:43], v[8:9], v[42:43]
	v_pk_mul_f32 v[44:45], v[2:3], v[44:45]
	v_mov_b32_e32 v31, v46
	v_mov_b32_e32 v30, v47

.LBB0_814:
	s_ashr_i32 s43, s42, 31
	s_lshl_b64 s[40:41], s[42:43], 3
	s_add_u32 s40, s0, s40
	s_addc_u32 s41, s1, s41
	s_load_dwordx2 s[94:95], s[40:41], 0x0
	s_add_i32 s42, s70, -1
	v_add_u32_e32 v0, s42, v158
	v_cmp_gt_u32_e32 vcc, s51, v0
	s_and_b64 s[52:53], s[6:7], vcc
	v_mov_b32_e32 v2, 0
	v_mov_b32_e32 v6, 0
	v_mov_b32_e32 v7, 0
	v_mov_b32_e32 v8, 0
	v_mov_b32_e32 v9, 0
	s_waitcnt lgkmcnt(0)
	s_barrier
	s_and_saveexec_b64 s[40:41], s[52:53]
	s_cbranch_execz .LBB0_816
	v_add_u32_e32 v4, s49, v0
	v_ashrrev_i32_e32 v5, 31, v4
	v_lshlrev_b64 v[4:5], 12, v[4:5]
	v_lshl_add_u64 v[4:5], v[72:73], 0, v[4:5]
	global_load_dwordx4 v[6:9], v[4:5], off nt
.LBB0_816:
	s_or_b64 exec, exec, s[40:41]
	v_add_u32_e32 v0, s42, v159
	v_cmp_gt_u32_e32 vcc, s51, v0
	s_and_b64 s[52:53], s[8:9], vcc
	v_mov_b32_e32 v3, 0
	v_mov_b32_e32 v4, 0
	v_mov_b32_e32 v5, 0
	s_and_saveexec_b64 s[40:41], s[52:53]
	s_cbranch_execz .LBB0_818
	v_add_u32_e32 v2, s49, v0
	v_ashrrev_i32_e32 v3, 31, v2
	v_lshlrev_b64 v[2:3], 12, v[2:3]
	v_lshl_add_u64 v[2:3], v[74:75], 0, v[2:3]
	global_load_dwordx4 v[2:5], v[2:3], off nt
.LBB0_818:
	s_or_b64 exec, exec, s[40:41]
	v_add_u32_e32 v0, s42, v160
	v_cmp_gt_u32_e32 vcc, s51, v0
	s_and_b64 s[52:53], s[10:11], vcc
	v_mov_b32_e32 v10, 0
	v_mov_b32_e32 v14, 0
	v_mov_b32_e32 v15, 0
	v_mov_b32_e32 v16, 0
	v_mov_b32_e32 v17, 0
	s_and_saveexec_b64 s[40:41], s[52:53]
	s_cbranch_execz .LBB0_820
	v_add_u32_e32 v12, s49, v0
	v_ashrrev_i32_e32 v13, 31, v12
	v_lshlrev_b64 v[12:13], 12, v[12:13]
	v_lshl_add_u64 v[12:13], v[76:77], 0, v[12:13]
	global_load_dwordx4 v[14:17], v[12:13], off nt
.LBB0_820:
	s_or_b64 exec, exec, s[40:41]
	v_add_u32_e32 v0, s42, v161
	v_cmp_gt_u32_e32 vcc, s51, v0
	s_and_b64 s[52:53], s[12:13], vcc
	v_mov_b32_e32 v11, 0
	v_mov_b32_e32 v12, 0
	v_mov_b32_e32 v13, 0
	s_and_saveexec_b64 s[40:41], s[52:53]
	s_cbranch_execz .LBB0_822
	v_add_u32_e32 v10, s49, v0
	v_ashrrev_i32_e32 v11, 31, v10
	v_lshlrev_b64 v[10:11], 12, v[10:11]
	v_lshl_add_u64 v[10:11], v[78:79], 0, v[10:11]
	global_load_dwordx4 v[10:13], v[10:11], off nt
.LBB0_822:
	s_or_b64 exec, exec, s[40:41]
	v_add_u32_e32 v0, s42, v162
	v_cmp_gt_u32_e32 vcc, s51, v0
	s_and_b64 s[52:53], s[14:15], vcc
	v_mov_b32_e32 v18, 0
	v_mov_b32_e32 v22, 0
	v_mov_b32_e32 v23, 0
	v_mov_b32_e32 v24, 0
	v_mov_b32_e32 v25, 0
	s_and_saveexec_b64 s[40:41], s[52:53]
	s_cbranch_execz .LBB0_824
	v_add_u32_e32 v20, s49, v0
	v_ashrrev_i32_e32 v21, 31, v20
	v_lshlrev_b64 v[20:21], 12, v[20:21]
	v_lshl_add_u64 v[20:21], v[80:81], 0, v[20:21]
	global_load_dwordx4 v[22:25], v[20:21], off nt
.LBB0_824:
	s_or_b64 exec, exec, s[40:41]
	v_add_u32_e32 v0, s42, v163
	v_cmp_gt_u32_e32 vcc, s51, v0
	s_and_b64 s[52:53], s[16:17], vcc
	v_mov_b32_e32 v19, 0
	v_mov_b32_e32 v20, 0
	v_mov_b32_e32 v21, 0
	s_and_saveexec_b64 s[40:41], s[52:53]
	s_cbranch_execz .LBB0_826
	v_add_u32_e32 v18, s49, v0
	v_ashrrev_i32_e32 v19, 31, v18
	v_lshlrev_b64 v[18:19], 12, v[18:19]
	v_lshl_add_u64 v[18:19], v[82:83], 0, v[18:19]
	global_load_dwordx4 v[18:21], v[18:19], off nt
.LBB0_826:
	s_or_b64 exec, exec, s[40:41]
	v_add_u32_e32 v0, s42, v164
	v_cmp_gt_u32_e32 vcc, s51, v0
	s_and_b64 s[52:53], s[18:19], vcc
	v_mov_b32_e32 v26, 0
	v_mov_b32_e32 v30, 0
	v_mov_b32_e32 v31, 0
	v_mov_b32_e32 v32, 0
	v_mov_b32_e32 v33, 0
	s_and_saveexec_b64 s[40:41], s[52:53]
	s_cbranch_execz .LBB0_828
	v_add_u32_e32 v28, s49, v0
	v_ashrrev_i32_e32 v29, 31, v28
	v_lshlrev_b64 v[28:29], 12, v[28:29]
	v_lshl_add_u64 v[28:29], v[84:85], 0, v[28:29]
	global_load_dwordx4 v[30:33], v[28:29], off nt
.LBB0_828:
	s_or_b64 exec, exec, s[40:41]
	v_add_u32_e32 v0, s42, v165
	v_cmp_gt_u32_e32 vcc, s51, v0
	s_and_b64 s[52:53], s[20:21], vcc
	v_mov_b32_e32 v27, 0
	v_mov_b32_e32 v28, 0
	v_mov_b32_e32 v29, 0
	s_and_saveexec_b64 s[40:41], s[52:53]
	s_cbranch_execz .LBB0_830
	v_add_u32_e32 v26, s49, v0
	v_ashrrev_i32_e32 v27, 31, v26
	v_lshlrev_b64 v[26:27], 12, v[26:27]
	v_lshl_add_u64 v[26:27], v[86:87], 0, v[26:27]
	global_load_dwordx4 v[26:29], v[26:27], off nt
.LBB0_830:
	s_or_b64 exec, exec, s[40:41]
	v_add_u32_e32 v0, s42, v166
	v_cmp_gt_u32_e32 vcc, s51, v0
	s_and_b64 s[52:53], s[22:23], vcc
	v_mov_b32_e32 v34, 0
	v_mov_b32_e32 v38, 0
	v_mov_b32_e32 v39, 0
	v_mov_b32_e32 v40, 0
	v_mov_b32_e32 v41, 0
	s_and_saveexec_b64 s[40:41], s[52:53]
	s_cbranch_execz .LBB0_832
	v_add_u32_e32 v36, s49, v0
	v_ashrrev_i32_e32 v37, 31, v36
	v_lshlrev_b64 v[36:37], 12, v[36:37]
	v_lshl_add_u64 v[36:37], v[88:89], 0, v[36:37]
	global_load_dwordx4 v[38:41], v[36:37], off nt
.LBB0_832:
	s_or_b64 exec, exec, s[40:41]
	v_add_u32_e32 v0, s42, v167
	v_cmp_gt_u32_e32 vcc, s51, v0
	s_and_b64 s[52:53], s[24:25], vcc
	v_mov_b32_e32 v35, 0
	v_mov_b32_e32 v36, 0
	v_mov_b32_e32 v37, 0
	s_and_saveexec_b64 s[40:41], s[52:53]
	s_cbranch_execz .LBB0_834
	v_add_u32_e32 v34, s49, v0
	v_ashrrev_i32_e32 v35, 31, v34
	v_lshlrev_b64 v[34:35], 12, v[34:35]
	v_lshl_add_u64 v[34:35], v[90:91], 0, v[34:35]
	global_load_dwordx4 v[34:37], v[34:35], off nt
.LBB0_834:
	s_or_b64 exec, exec, s[40:41]
	v_add_u32_e32 v0, s42, v168
	v_cmp_gt_u32_e32 vcc, s51, v0
	s_and_b64 s[52:53], s[26:27], vcc
	v_mov_b32_e32 v42, 0
	v_mov_b32_e32 v46, 0
	v_mov_b32_e32 v47, 0
	v_mov_b32_e32 v48, 0
	v_mov_b32_e32 v49, 0
	s_and_saveexec_b64 s[40:41], s[52:53]
	s_cbranch_execz .LBB0_836
	v_add_u32_e32 v44, s49, v0
	v_ashrrev_i32_e32 v45, 31, v44
	v_lshlrev_b64 v[44:45], 12, v[44:45]
	v_lshl_add_u64 v[44:45], v[92:93], 0, v[44:45]
	global_load_dwordx4 v[46:49], v[44:45], off nt
.LBB0_836:
	s_or_b64 exec, exec, s[40:41]
	v_add_u32_e32 v0, s42, v169
	v_cmp_gt_u32_e32 vcc, s51, v0
	s_and_b64 s[52:53], s[28:29], vcc
	v_mov_b32_e32 v43, 0
	v_mov_b32_e32 v44, 0
	v_mov_b32_e32 v45, 0
	s_and_saveexec_b64 s[40:41], s[52:53]
	s_cbranch_execz .LBB0_838
	v_add_u32_e32 v42, s49, v0
	v_ashrrev_i32_e32 v43, 31, v42
	v_lshlrev_b64 v[42:43], 12, v[42:43]
	v_lshl_add_u64 v[42:43], v[94:95], 0, v[42:43]
	global_load_dwordx4 v[42:45], v[42:43], off nt
.LBB0_838:
	s_or_b64 exec, exec, s[40:41]
	v_add_u32_e32 v0, s42, v170
	v_cmp_gt_u32_e32 vcc, s51, v0
	s_and_b64 s[42:43], s[30:31], vcc
	v_mov_b32_e32 v50, 0
	v_mov_b32_e32 v51, 0
	v_mov_b32_e32 v52, 0
	v_mov_b32_e32 v53, 0
	s_and_saveexec_b64 s[40:41], s[42:43]
	s_cbranch_execz .LBB0_852
	v_add_u32_e32 v50, s49, v0
	v_ashrrev_i32_e32 v51, 31, v50
	v_lshlrev_b64 v[50:51], 12, v[50:51]
	v_lshl_add_u64 v[50:51], v[96:97], 0, v[50:51]
	global_load_dwordx4 v[50:53], v[50:51], off nt
	s_or_b64 exec, exec, s[40:41]
	s_and_saveexec_b64 s[40:41], s[6:7]
	s_cbranch_execnz .LBB0_853

.LBB0_928:
	v_mbcnt_lo_u32_b32 v176, -1, 0
	v_mbcnt_hi_u32_b32 v176, -1, v176
	s_getreg_b32 s6, hwreg(HW_REG_HW_ID, 0, 6)
	s_lshl_b32 s6, s6, 2
	s_and_b32 s6, s6, 0xfc
	s_or_b32 s6, s6, 0x27100
	v_mov_b32_e32 v0, s6
	s_lshl_b32 s6, s17, 5
	s_and_b32 s6, s6, 0xe0
	s_ashr_i32 s7, s17, 3
	s_or_b32 s8, s6, s7
	s_mov_b32 s6, 35
	ds_read_b32 v0, v0
	s_ashr_i32 s7, s6, 31
	s_lshl_b64 s[6:7], s[6:7], 3
	s_add_u32 s6, s0, s6
	s_addc_u32 s7, s1, s7
	s_load_dwordx2 s[10:11], s[6:7], 0x0
	s_add_i32 s6, s8, s16
	s_ashr_i32 s7, s6, 31
	s_waitcnt lgkmcnt(0)
	v_readfirstlane_b32 s9, v0
	s_lshl_b64 s[12:13], s[6:7], 14
	s_waitcnt vmcnt(0)
	v_lshl_or_b32 v0, s9, 6, v176
	s_add_u32 s9, s10, s12
	s_addc_u32 s10, s11, s13
	v_lshlrev_b32_e32 v2, 3, v0
	s_add_u32 s9, s9, 0x1003ff0
	v_ashrrev_i32_e32 v3, 31, v2
	s_addc_u32 s10, s10, 0
	v_lshlrev_b64 v[38:39], 1, v[2:3]
	v_mov_b32_e32 v3, s10
	v_sub_co_u32_e32 v4, vcc, s9, v38
	v_add_u32_e32 v2, 0x1000, v2
	s_nop 0
	v_subb_co_u32_e32 v5, vcc, v3, v39, vcc
	v_ashrrev_i32_e32 v3, 31, v2
	v_lshlrev_b64 v[2:3], 1, v[2:3]
	v_mov_b32_e32 v7, s10
	v_sub_co_u32_e32 v6, vcc, s9, v2
	s_mov_b32 s10, 35
	s_nop 0
	v_subb_co_u32_e32 v7, vcc, v7, v3, vcc
	s_barrier
	global_load_dwordx4 v[2:5], v[4:5], off nt
	s_nop 0
	global_load_dwordx4 v[6:9], v[6:7], off nt
	s_ashr_i32 s11, s10, 31
	s_lshl_b64 s[10:11], s[10:11], 3
	s_add_u32 s10, s0, s10
	s_addc_u32 s11, s1, s11
	s_load_dwordx2 s[12:13], s[10:11], 0x0
	s_ashr_i32 s9, s8, 31
	s_lshl_b64 s[10:11], s[8:9], 13
	s_mov_b32 s9, 0x34600000
	v_lshl_add_u32 v46, v0, 4, 0
	s_waitcnt lgkmcnt(0)
	s_add_u32 s12, s12, s10
	s_addc_u32 s13, s13, s11
	v_lshl_add_u64 v[10:11], s[12:13], 0, v[38:39]
	v_add_co_u32_e32 v10, vcc, s83, v10
	s_mov_b32 s12, 35
	s_nop 0
	v_addc_co_u32_e32 v11, vcc, 0, v11, vcc
	global_load_dwordx4 v[10:13], v[10:11], off nt
	s_ashr_i32 s13, s12, 31
	s_lshl_b64 s[12:13], s[12:13], 3
	s_add_u32 s12, s0, s12
	s_addc_u32 s13, s1, s13
	s_load_dwordx2 s[12:13], s[12:13], 0x0
	v_add_u32_e32 v47, 0x10100, v46
	s_waitcnt lgkmcnt(0)
	s_add_u32 s12, s12, s10
	s_addc_u32 s13, s13, s11
	v_lshl_add_u64 v[14:15], s[12:13], 0, v[38:39]
	v_add_co_u32_e32 v14, vcc, s9, v14
	s_mov_b32 s12, 35
	s_nop 0
	v_addc_co_u32_e32 v15, vcc, 0, v15, vcc
	global_load_dwordx4 v[14:17], v[14:15], off nt
	s_ashr_i32 s13, s12, 31
	s_lshl_b64 s[12:13], s[12:13], 3
	s_add_u32 s12, s0, s12
	s_addc_u32 s13, s1, s13
	s_load_dwordx2 s[12:13], s[12:13], 0x0
	s_mov_b32 s9, 0x34800000
	s_waitcnt lgkmcnt(0)
	s_add_u32 s12, s12, s10
	s_addc_u32 s13, s13, s11
	v_lshl_add_u64 v[18:19], s[12:13], 0, v[38:39]
	v_add_co_u32_e32 v18, vcc, s9, v18
	s_mov_b32 s12, 35
	s_nop 0
	v_addc_co_u32_e32 v19, vcc, 0, v19, vcc
	global_load_dwordx4 v[18:21], v[18:19], off nt
	s_ashr_i32 s13, s12, 31
	s_lshl_b64 s[12:13], s[12:13], 3
	s_add_u32 s12, s0, s12
	s_addc_u32 s13, s1, s13
	s_load_dwordx2 s[12:13], s[12:13], 0x0
	s_mov_b32 s9, 0x34a00000
	s_waitcnt lgkmcnt(0)
	s_add_u32 s12, s12, s10
	s_addc_u32 s13, s13, s11
	v_lshl_add_u64 v[22:23], s[12:13], 0, v[38:39]
	v_add_co_u32_e32 v22, vcc, s9, v22
	s_mov_b32 s12, 35
	s_nop 0
	v_addc_co_u32_e32 v23, vcc, 0, v23, vcc
	global_load_dwordx4 v[22:25], v[22:23], off nt
	s_ashr_i32 s13, s12, 31
	s_lshl_b64 s[12:13], s[12:13], 3
	s_add_u32 s12, s0, s12
	s_addc_u32 s13, s1, s13
	s_load_dwordx2 s[12:13], s[12:13], 0x0
	s_mov_b32 s9, 0x34c00000
	s_waitcnt lgkmcnt(0)
	s_add_u32 s12, s12, s10
	s_addc_u32 s13, s13, s11
	v_lshl_add_u64 v[26:27], s[12:13], 0, v[38:39]
	v_add_co_u32_e32 v26, vcc, s9, v26
	s_mov_b32 s12, 35
	s_nop 0
	v_addc_co_u32_e32 v27, vcc, 0, v27, vcc
	global_load_dwordx4 v[26:29], v[26:27], off nt
	s_ashr_i32 s13, s12, 31
	s_lshl_b64 s[12:13], s[12:13], 3
	s_add_u32 s12, s0, s12
	s_addc_u32 s13, s1, s13
	s_load_dwordx2 s[12:13], s[12:13], 0x0
	s_mov_b32 s9, 0x34e00000
	s_waitcnt lgkmcnt(0)
	s_add_u32 s12, s12, s10
	s_addc_u32 s13, s13, s11
	v_lshl_add_u64 v[30:31], s[12:13], 0, v[38:39]
	v_add_co_u32_e32 v30, vcc, s9, v30
	s_mov_b32 s12, 35
	s_nop 0
	v_addc_co_u32_e32 v31, vcc, 0, v31, vcc
	global_load_dwordx4 v[30:33], v[30:31], off nt
	s_ashr_i32 s13, s12, 31
	s_lshl_b64 s[12:13], s[12:13], 3
	s_add_u32 s12, s0, s12
	s_addc_u32 s13, s1, s13
	s_load_dwordx2 s[12:13], s[12:13], 0x0
	s_mov_b32 s9, 0x35000000
	s_waitcnt lgkmcnt(0)
	s_add_u32 s12, s12, s10
	s_addc_u32 s13, s13, s11
	v_lshl_add_u64 v[34:35], s[12:13], 0, v[38:39]
	v_add_co_u32_e32 v34, vcc, s9, v34
	s_mov_b32 s12, 35
	s_nop 0
	v_addc_co_u32_e32 v35, vcc, 0, v35, vcc
	global_load_dwordx4 v[34:37], v[34:35], off nt
	s_ashr_i32 s13, s12, 31
	s_lshl_b64 s[12:13], s[12:13], 3
	s_add_u32 s12, s0, s12
	s_addc_u32 s13, s1, s13
	s_load_dwordx2 s[12:13], s[12:13], 0x0
	s_mov_b32 s9, 0x35200000
	s_waitcnt lgkmcnt(0)
	s_add_u32 s10, s12, s10
	s_addc_u32 s11, s13, s11
	v_lshl_add_u64 v[38:39], s[10:11], 0, v[38:39]
	v_add_co_u32_e32 v38, vcc, s9, v38
	v_readfirstlane_b32 s9, v0
	s_nop 0
	v_addc_co_u32_e32 v39, vcc, 0, v39, vcc
	global_load_dwordx4 v[38:41], v[38:39], off nt
	v_cmp_gt_i32_e32 vcc, 32, v0
	s_waitcnt vmcnt(9)
	v_alignbit_b32 v42, v5, v5, 16
	v_alignbit_b32 v43, v4, v4, 16
	v_alignbit_b32 v44, v3, v3, 16
	v_alignbit_b32 v45, v2, v2, 16
	s_waitcnt vmcnt(8)
	v_alignbit_b32 v2, v9, v9, 16
	v_alignbit_b32 v3, v8, v8, 16
	v_alignbit_b32 v4, v7, v7, 16
	v_alignbit_b32 v5, v6, v6, 16
	ds_write_b128 v46, v[42:45]
	ds_write_b128 v46, v[2:5] offset:8192
	s_waitcnt vmcnt(7)
	ds_write_b128 v47, v[10:13]
	s_waitcnt vmcnt(6)
	ds_write_b128 v47, v[14:17] offset:8224
	s_waitcnt vmcnt(5)
	ds_write_b128 v47, v[18:21] offset:16448
	s_waitcnt vmcnt(4)
	ds_write_b128 v47, v[22:25] offset:24672
	s_waitcnt vmcnt(3)
	ds_write_b128 v47, v[26:29] offset:32896
	s_waitcnt vmcnt(2)
	ds_write_b128 v47, v[30:33] offset:41120
	s_waitcnt vmcnt(1)
	ds_write_b128 v47, v[34:37] offset:49344
	s_waitcnt vmcnt(0)
	ds_write_b128 v47, v[38:41] offset:57568
	s_and_saveexec_b64 s[10:11], vcc
	v_lshl_add_u32 v2, v0, 2, 0
	v_add_u32_e32 v2, 0x20200, v2
	ds_write_b32 v2, v1
	s_or_b64 exec, exec, s[10:11]
	s_movk_i32 s10, 0x3000
	v_cmp_gt_i32_e32 vcc, s10, v0
	s_waitcnt lgkmcnt(0)
	s_barrier
	v_lshlrev_b32_e32 v2, 2, v0
	v_cmp_gt_u32_e32 vcc, 511, v0
	s_movk_i32 s14, 0x1fe
	v_cmp_gt_u32_e64 s[12:13], s14, v0
	ds_read_b32 v3, v2
	ds_read_b32 v4, v2 offset:4
	ds_read_b32 v5, v2 offset:8
	ds_read_b32 v6, v2 offset:2048
	ds_read_b32 v7, v2 offset:2052
	ds_read_b32 v8, v2 offset:2056
	ds_read_b32 v9, v2 offset:4096
	ds_read_b32 v10, v2 offset:4100
	ds_read_b32 v11, v2 offset:4104
	ds_read_b32 v12, v2 offset:6144
	ds_read_b32 v13, v2 offset:6148
	ds_read_b32 v14, v2 offset:6152
	s_waitcnt lgkmcnt(0)
	v_alignbit_b32 v15, v4, v3, 16
	v_alignbit_b32 v16, v5, v4, 16
	v_alignbit_b32 v17, v7, v6, 16
	v_alignbit_b32 v18, v8, v7, 16
	v_alignbit_b32 v19, v10, v9, 16
	v_alignbit_b32 v20, v11, v10, 16
	v_alignbit_b32 v21, v13, v12, 16
	v_alignbit_b32 v22, v14, v13, 16
	ds_write_b32 v2, v15 offset:16448
	ds_write_b32 v2, v4 offset:32896
	ds_write_b32 v2, v16 offset:49344
	ds_write_b32 v2, v17 offset:18496
	ds_write_b32 v2, v7 offset:34944
	ds_write_b32 v2, v18 offset:51392
	ds_write_b32 v2, v19 offset:20544
	ds_write_b32 v2, v10 offset:36992
	ds_write_b32 v2, v20 offset:53440
	ds_write_b32 v2, v21 offset:22592
	ds_write_b32 v2, v13 offset:39040
	ds_write_b32 v2, v22 offset:55488
	ds_read_b32 v3, v2 offset:8192
	ds_read_b32 v4, v2 offset:8196
	ds_read_b32 v5, v2 offset:8200
	ds_read_b32 v6, v2 offset:10240
	ds_read_b32 v7, v2 offset:10244
	ds_read_b32 v8, v2 offset:10248
	ds_read_b32 v9, v2 offset:12288
	ds_read_b32 v10, v2 offset:12292
	ds_read_b32 v11, v2 offset:12296
	ds_read_b32 v12, v2 offset:14336
	ds_read_b32 v13, v2 offset:14340
	ds_read_b32 v14, v2 offset:14344
	s_waitcnt lgkmcnt(0)
	v_cndmask_b32_e32 v13, v1, v13, vcc
	v_cndmask_b32_e64 v14, v1, v14, s[12:13]
	v_alignbit_b32 v15, v4, v3, 16
	v_alignbit_b32 v16, v5, v4, 16
	v_alignbit_b32 v17, v7, v6, 16
	v_alignbit_b32 v18, v8, v7, 16
	v_alignbit_b32 v19, v10, v9, 16
	v_alignbit_b32 v20, v11, v10, 16
	v_alignbit_b32 v21, v13, v12, 16
	v_alignbit_b32 v22, v14, v13, 16
	ds_write_b32 v2, v15 offset:24640
	ds_write_b32 v2, v4 offset:41088
	ds_write_b32 v2, v16 offset:57536
	ds_write_b32 v2, v17 offset:26688
	ds_write_b32 v2, v7 offset:43136
	ds_write_b32 v2, v18 offset:59584
	ds_write_b32 v2, v19 offset:28736
	ds_write_b32 v2, v10 offset:45184
	ds_write_b32 v2, v20 offset:61632
	ds_write_b32 v2, v21 offset:30784
	ds_write_b32 v2, v13 offset:47232
	ds_write_b32 v2, v22 offset:63680
.LBB0_935:
	s_mov_b32 s10, 35
	s_waitcnt lgkmcnt(0)
	s_barrier
	s_ashr_i32 s11, s10, 31
	s_ashr_i32 s12, s9, 6
	s_lshl_b64 s[10:11], s[10:11], 3
	s_add_u32 s10, s0, s10
	s_addc_u32 s11, s1, s11
	s_load_dwordx2 s[10:11], s[10:11], 0x0
	v_bfe_u32 v9, v176, 1, 3
	v_lshl_add_u32 v2, v9, 8, s8
	v_and_b32_e32 v177, 1, v176
	v_ashrrev_i32_e32 v3, 31, v2
	v_bfe_u32 v8, v0, 4, 2
	v_lshlrev_b64 v[4:5], 13, v[2:3]
	v_lshlrev_b32_e32 v6, 6, v177
	v_lshlrev_b32_e32 v172, 3, v8
	s_waitcnt lgkmcnt(0)
	v_lshl_add_u64 v[4:5], s[10:11], 0, v[4:5]
	v_mov_b32_e32 v173, v1
	v_lshl_or_b32 v6, s12, 9, v6
	v_lshl_add_u64 v[4:5], v[4:5], 0, v[172:173]
	v_ashrrev_i32_e32 v7, 31, v6
	v_lshl_add_u64 v[4:5], v[6:7], 1, v[4:5]
	s_mov_b64 s[8:9], 0x35400000
	v_lshl_add_u64 v[6:7], v[4:5], 0, s[8:9]
	s_mov_b32 s8, 0x35400000
	v_add_co_u32_e32 v4, vcc, s8, v4
	s_movk_i32 s8, 0xffc
	s_nop 0
	v_addc_co_u32_e32 v5, vcc, 0, v5, vcc
	global_load_dwordx2 v[168:169], v[6:7], off offset:32 nt
	global_load_dwordx2 v[166:167], v[6:7], off offset:64 nt
	global_load_dwordx2 v[164:165], v[6:7], off offset:96 nt
	global_load_dwordx2 v[162:163], v[6:7], off offset:256 nt
	global_load_dwordx2 v[160:161], v[6:7], off offset:288 nt
	global_load_dwordx2 v[158:159], v[6:7], off offset:320 nt
	global_load_dwordx2 v[156:157], v[6:7], off offset:352 nt
	global_load_dwordx2 v[154:155], v[6:7], off offset:512 nt
	global_load_dwordx2 v[152:153], v[6:7], off offset:544 nt
	global_load_dwordx2 v[150:151], v[6:7], off offset:576 nt
	global_load_dwordx2 v[148:149], v[6:7], off offset:608 nt
	global_load_dwordx2 v[146:147], v[6:7], off offset:768 nt
	global_load_dwordx2 v[170:171], v[4:5], off nt
	global_load_dwordx2 v[144:145], v[6:7], off offset:800 nt
	global_load_dwordx2 v[142:143], v[6:7], off offset:832 nt
	global_load_dwordx2 v[140:141], v[6:7], off offset:864 nt
	v_and_b32_e32 v4, 15, v176
	v_mov_b32_e32 v5, 0xfff
	v_lshrrev_b32_e32 v173, 4, v0
	v_bitop3_b32 v0, v4, 3, v5 bitop3:0x48
	v_bitop3_b32 v4, v4, s8, v5 bitop3:0x48
	v_add_u32_e32 v4, v172, v4
	v_mul_u32_u24_e32 v178, 0x2020, v9
	v_lshlrev_b32_e32 v179, 4, v8
	v_lshlrev_b64 v[174:175], 12, v[2:3]
	v_mul_u32_u24_e32 v0, 0x4040, v0
	s_lshl_b32 s18, s12, 3
	s_sub_i32 s20, s18, 63
	v_lshl_add_u32 v180, v4, 1, v0
	s_lshl_b32 s8, s20, 7
	v_subrev_u32_e32 v0, s8, v180
	v_add_u32_e32 v0, 0, v0
	v_subrev_u32_e32 v2, 32, v0
	ds_read_b64 v[124:125], v0 offset:64
	ds_read_b64 v[126:127], v0 offset:72
	ds_read_b64 v[128:129], v0 offset:32
	ds_read_b64 v[130:131], v0 offset:40
	ds_read_b64 v[132:133], v0
	ds_read_b64 v[134:135], v0 offset:8
	ds_read_b64 v[136:137], v2
	v_subrev_u32_e32 v2, 24, v0
	ds_read_b64 v[138:139], v2
	v_subrev_u32_e32 v2, 64, v0
	ds_read_b64 v[68:69], v2
	v_subrev_u32_e32 v2, 56, v0
	ds_read_b64 v[70:71], v2
	v_add_u32_e32 v2, 0xffffffa0, v0
	v_add_u32_e32 v0, 0xffffffa8, v0
	ds_read_b64 v[72:73], v2
	ds_read_b64 v[74:75], v0
	v_lshlrev_b32_e32 v0, 7, v177
	s_movk_i32 s8, 0x2020
	v_mad_u32_u24 v0, v9, s8, v0
	s_mov_b32 s8, 0x12080
	v_mov_b32_e32 v2, v1
	v_mov_b32_e32 v3, v1
	v_add3_u32 v184, v0, v179, s8
	v_mov_b32_e32 v0, v1
	v_mov_b64_e32 v[6:7], v[2:3]
	v_mov_b64_e32 v[22:23], v[2:3]
	v_mov_b64_e32 v[38:39], v[2:3]
	v_mov_b64_e32 v[54:55], v[2:3]
	v_mov_b64_e32 v[10:11], v[2:3]
	v_mov_b64_e32 v[26:27], v[2:3]
	v_mov_b64_e32 v[42:43], v[2:3]
	v_mov_b64_e32 v[58:59], v[2:3]
	v_mov_b64_e32 v[14:15], v[2:3]
	v_mov_b64_e32 v[30:31], v[2:3]
	v_mov_b64_e32 v[46:47], v[2:3]
	v_mov_b64_e32 v[62:63], v[2:3]
	v_mov_b64_e32 v[18:19], v[2:3]
	v_mov_b64_e32 v[34:35], v[2:3]
	v_mov_b64_e32 v[50:51], v[2:3]
	v_mov_b64_e32 v[66:67], v[2:3]
	s_or_b32 s19, s18, 7
	v_subrev_u32_e32 v183, 32, v180
	v_subrev_u32_e32 v182, 64, v180
	v_add_u32_e32 v181, 0xffffffa0, v180
	s_movk_i32 s21, 0x46
	v_mov_b64_e32 v[4:5], v[0:1]
	v_mov_b64_e32 v[20:21], v[0:1]
	v_mov_b64_e32 v[36:37], v[0:1]
	v_mov_b64_e32 v[52:53], v[0:1]
	v_mov_b64_e32 v[8:9], v[0:1]
	v_mov_b64_e32 v[24:25], v[0:1]
	v_mov_b64_e32 v[40:41], v[0:1]
	v_mov_b64_e32 v[56:57], v[0:1]
	v_mov_b64_e32 v[12:13], v[0:1]
	v_mov_b64_e32 v[28:29], v[0:1]
	v_mov_b64_e32 v[44:45], v[0:1]
	v_mov_b64_e32 v[60:61], v[0:1]
	v_mov_b64_e32 v[16:17], v[0:1]
	v_mov_b64_e32 v[32:33], v[0:1]
	v_mov_b64_e32 v[48:49], v[0:1]
	v_mov_b64_e32 v[64:65], v[0:1]

.LBB0_1210:
	s_mul_i32 s6, s73, 10
	s_add_i32 s22, s6, 5
	s_movk_i32 s6, 0x48
	s_ashr_i32 s7, s6, 31
	s_lshl_b64 s[6:7], s[6:7], 2
	s_add_u32 s6, s0, s6
	s_addc_u32 s7, s1, s7
	s_load_dwordx2 s[8:9], s[6:7], 0x0
	s_waitcnt lgkmcnt(0)
	s_cmp_le_i32 s8, s22
	s_cselect_b64 s[6:7], -1, 0
	s_cmp_lt_i32 s22, s9
	s_cselect_b64 s[8:9], -1, 0
	s_and_b64 s[6:7], s[6:7], s[8:9]
	s_andn2_b64 vcc, exec, s[6:7]
	s_cbranch_vccnz .LBB0_1360
	v_mbcnt_lo_u32_b32 v0, -1, 0
	v_mbcnt_hi_u32_b32 v0, -1, v0
	s_getreg_b32 s6, hwreg(HW_REG_HW_ID, 0, 6)
	s_lshl_b32 s6, s6, 2
	s_and_b32 s6, s6, 0xfc
	s_or_b32 s6, s6, 0x27100
	s_waitcnt vmcnt(0)
	v_mov_b32_e32 v2, s6
	s_mov_b32 s6, 35
	ds_read_b32 v18, v2
	s_ashr_i32 s7, s6, 31
	s_lshl_b64 s[6:7], s[6:7], 3
	s_add_u32 s8, s0, s6
	s_mov_b32 s6, 24
	s_addc_u32 s9, s1, s7
	s_ashr_i32 s7, s6, 31
	s_lshl_b64 s[6:7], s[6:7], 3
	s_add_u32 s6, s0, s6
	s_addc_u32 s7, s1, s7
	s_load_dwordx2 s[6:7], s[6:7], 0x0
	s_lshl_b32 s70, s73, 10
	s_lshl_b64 s[10:11], s[70:71], 2
	v_and_b32_e32 v86, 63, v0
	v_lshlrev_b32_e32 v14, 6, v86
	s_waitcnt lgkmcnt(0)
	s_add_u32 s6, s6, s10
	s_addc_u32 s7, s7, s11
	s_mov_b32 s10, 35
	global_load_dwordx4 v[2:5], v14, s[6:7] offset:48
	global_load_dwordx4 v[6:9], v14, s[6:7] offset:32
	global_load_dwordx4 v[10:13], v14, s[6:7] offset:16
	s_nop 0
	global_load_dwordx4 v[14:17], v14, s[6:7]
	s_ashr_i32 s11, s10, 31
	s_lshl_b64 s[6:7], s[10:11], 3
	s_add_u32 s6, s0, s6
	s_addc_u32 s7, s1, s7
	s_load_dwordx2 s[6:7], s[6:7], 0x0
	v_readfirstlane_b32 s10, v18
	v_readlane_b32 s12, v254, 18
	v_readlane_b32 s13, v254, 19
	v_lshl_or_b32 v34, s10, 6, v0
	s_waitcnt lgkmcnt(0)
	s_add_u32 s10, s6, 0x34400000
	v_cndmask_b32_e64 v18, 0, 1, s[12:13]
	v_lshlrev_b32_e32 v0, 4, v0
	v_add_u32_e32 v37, 0x200, v34
	v_add_u32_e32 v36, 0x400, v34
	v_add_u32_e32 v35, 0x600, v34
	s_addc_u32 s11, s7, 0
	v_cmp_ne_u32_e64 s[6:7], 1, v18
	s_andn2_b64 vcc, exec, s[12:13]
	v_ashrrev_i32_e32 v87, 3, v34
	v_and_b32_e32 v0, 0x70, v0
	v_ashrrev_i32_e32 v88, 3, v37
	v_ashrrev_i32_e32 v89, 3, v36
	v_ashrrev_i32_e32 v90, 3, v35
	s_barrier
	s_cbranch_vccnz .LBB0_1213
	v_readlane_b32 s12, v254, 59
	s_add_u32 s12, s10, s12
	s_addc_u32 s13, s11, 0
	v_lshl_add_u64 v[26:27], s[12:13], 0, v[0:1]
	v_readlane_b32 s12, v254, 20
	s_nop 1
	v_add_u32_e32 v18, s12, v87
	v_add_u32_e32 v20, s12, v88
	v_add_u32_e32 v28, s12, v89
	v_add_u32_e32 v30, s12, v90
	v_ashrrev_i32_e32 v19, 31, v18
	v_ashrrev_i32_e32 v21, 31, v20
	v_ashrrev_i32_e32 v29, 31, v28
	v_ashrrev_i32_e32 v31, 31, v30
	v_lshlrev_b64 v[18:19], 13, v[18:19]
	v_lshlrev_b64 v[20:21], 13, v[20:21]
	v_lshlrev_b64 v[28:29], 13, v[28:29]
	v_lshlrev_b64 v[30:31], 13, v[30:31]
	v_lshl_add_u64 v[18:19], v[26:27], 0, v[18:19]
	v_lshl_add_u64 v[22:23], v[26:27], 0, v[20:21]
	v_lshl_add_u64 v[28:29], v[26:27], 0, v[28:29]
	v_lshl_add_u64 v[30:31], v[26:27], 0, v[30:31]
	global_load_dwordx4 v[18:21], v[18:19], off nt
	s_nop 0
	global_load_dwordx4 v[22:25], v[22:23], off nt
	s_nop 0
	global_load_dwordx4 v[26:29], v[28:29], off nt
	s_nop 0
	global_load_dwordx4 v[30:33], v[30:31], off nt

.LBB0_1216:
	s_mul_i32 s14, s23, 0x8100
	s_add_i32 s17, s14, 0
	v_add_u32_e32 v34, s17, v95
	v_add3_u32 v34, v34, v96, v0
	s_waitcnt vmcnt(3)
	ds_write_b128 v34, v[18:21]
	v_add_u32_e32 v34, s17, v97
	v_add3_u32 v34, v34, v98, v0
	s_waitcnt vmcnt(2)
	ds_write_b128 v34, v[22:25]
	v_add_u32_e32 v34, s17, v99
	s_add_i32 s24, s16, s3
	v_add3_u32 v34, v34, v100, v0
	s_cmpk_gt_i32 s24, 0x1ff
	s_waitcnt vmcnt(1)
	ds_write_b128 v34, v[26:29]
	v_add_u32_e32 v34, s17, v101
	s_cselect_b64 s[14:15], -1, 0
	v_add3_u32 v34, v34, v102, v0
	s_and_b64 vcc, exec, s[14:15]
	s_waitcnt vmcnt(0)
	ds_write_b128 v34, v[30:33]
	s_waitcnt lgkmcnt(0)
	s_barrier
	s_cbranch_vccnz .LBB0_1218
	s_lshl_b32 s18, s24, 2
	s_and_b32 s18, s18, 0xffffff00
	s_lshl_b32 s19, s24, 7
	v_add_u32_e32 v18, s18, v87
	v_add_u32_e32 v20, s18, v88
	v_add_u32_e32 v28, s18, v89
	v_add_u32_e32 v30, s18, v90
	s_and_b32 s70, s19, 0x1f80
	v_ashrrev_i32_e32 v19, 31, v18
	v_ashrrev_i32_e32 v21, 31, v20
	v_ashrrev_i32_e32 v29, 31, v28
	v_ashrrev_i32_e32 v31, 31, v30
	v_lshl_add_u64 v[26:27], v[66:67], 0, s[70:71]
	v_lshlrev_b64 v[18:19], 13, v[18:19]
	v_lshlrev_b64 v[20:21], 13, v[20:21]
	v_lshlrev_b64 v[28:29], 13, v[28:29]
	v_lshlrev_b64 v[30:31], 13, v[30:31]
	v_lshl_add_u64 v[18:19], v[26:27], 0, v[18:19]
	v_lshl_add_u64 v[22:23], v[26:27], 0, v[20:21]
	v_lshl_add_u64 v[28:29], v[26:27], 0, v[28:29]
	v_lshl_add_u64 v[30:31], v[26:27], 0, v[30:31]
	global_load_dwordx4 v[18:21], v[18:19], off nt
	s_nop 0
	global_load_dwordx4 v[22:25], v[22:23], off nt
	s_nop 0
	global_load_dwordx4 v[26:29], v[28:29], off nt
	s_nop 0
	global_load_dwordx4 v[30:33], v[30:31], off nt

.LBB0_1222:
	s_or_saveexec_b64 s[18:19], s[18:19]
	v_or_b32_e32 v70, s20, v103
	v_ashrrev_i32_e32 v71, 31, v70
	v_lshlrev_b64 v[34:35], 11, v[70:71]
	v_lshl_add_u64 v[76:77], v[68:69], 0, v[34:35]
	s_xor_b64 exec, exec, s[18:19]
	s_cbranch_execz .LBB0_1224
	global_load_dwordx4 v[58:61], v[76:77], off offset:16 nt
	global_load_dwordx4 v[62:65], v[76:77], off nt

.LBB0_1226:
	s_or_saveexec_b64 s[18:19], s[18:19]
	v_or_b32_e32 v34, 1, v70
	v_ashrrev_i32_e32 v35, 31, v34
	v_lshlrev_b64 v[34:35], 11, v[34:35]
	v_lshl_add_u64 v[74:75], v[68:69], 0, v[34:35]
	s_xor_b64 exec, exec, s[18:19]
	s_cbranch_execz .LBB0_1228
	global_load_dwordx4 v[50:53], v[74:75], off offset:16 nt
	global_load_dwordx4 v[54:57], v[74:75], off nt

.LBB0_1230:
	s_or_saveexec_b64 s[18:19], s[18:19]
	v_or_b32_e32 v34, 2, v70
	v_ashrrev_i32_e32 v35, 31, v34
	v_lshlrev_b64 v[34:35], 11, v[34:35]
	v_lshl_add_u64 v[72:73], v[68:69], 0, v[34:35]
	s_xor_b64 exec, exec, s[18:19]
	s_cbranch_execz .LBB0_1232
	global_load_dwordx4 v[42:45], v[72:73], off offset:16 nt
	global_load_dwordx4 v[46:49], v[72:73], off nt

.LBB0_1234:
	s_or_saveexec_b64 s[18:19], s[18:19]
	v_or_b32_e32 v70, 3, v70
	v_ashrrev_i32_e32 v71, 31, v70
	v_lshlrev_b64 v[70:71], 11, v[70:71]
	v_lshl_add_u64 v[70:71], v[68:69], 0, v[70:71]
	s_xor_b64 exec, exec, s[18:19]
	s_cbranch_execz .LBB0_1236
	global_load_dwordx4 v[34:37], v[70:71], off offset:16 nt
	global_load_dwordx4 v[38:41], v[70:71], off nt
